# v27
# speedup vs baseline: 1.0027x; 1.0027x over previous
.LBB2_35:
	s_lshl_b32 s28, s27, 2
	v_add_u32_e32 v79, s28, v3
	v_lshl_add_u32 v79, v79, 2, v2
	ds_read_b32 v80, v79 offset:15360
	ds_read_b32 v81, v79 offset:15364
	ds_read_b32 v82, v79 offset:15368
	ds_read_b32 v79, v79 offset:15372
	s_waitcnt vmcnt(10)
	v_cvt_pk_f16_f32 v10, v61, v62
	v_perm_b32 v11, v40, v38, s23
	v_dot2c_f32_f16_e32 v60, v11, v10
	v_perm_b32 v11, v40, v38, s24
	v_dot2c_f32_f16_e32 v42, v11, v10
	v_perm_b32 v11, v40, v38, s25
	v_dot2c_f32_f16_e32 v43, v11, v10
	v_perm_b32 v11, v40, v38, s26
	v_dot2c_f32_f16_e32 v36, v11, v10
	v_perm_b32 v11, v41, v39, s23
	v_dot2c_f32_f16_e32 v37, v11, v10
	v_perm_b32 v11, v41, v39, s24
	v_dot2c_f32_f16_e32 v30, v11, v10
	v_perm_b32 v11, v41, v39, s25
	v_dot2c_f32_f16_e32 v31, v11, v10
	v_perm_b32 v11, v41, v39, s26
	v_dot2c_f32_f16_e32 v53, v11, v10
	v_dot2c_f32_f16_e32 v45, 0x3c003c00, v10
	v_cmp_lt_i32_e32 vcc, s28, v5
	s_or_b32 s29, s28, 1
	s_or_b32 s30, s28, 2
	s_waitcnt lgkmcnt(0)
	v_cndmask_b32_e32 v87, v9, v80, vcc
	v_cmp_lt_i32_e32 vcc, s29, v5
	s_or_b32 s31, s28, 3
	s_nop 0
	v_cndmask_b32_e32 v88, v9, v81, vcc
	v_cmp_lt_i32_e32 vcc, s30, v5
	v_lshl_or_b32 v83, v87, 7, v66
	v_lshlrev_b32_e32 v87, 2, v87
	v_cndmask_b32_e32 v89, v9, v82, vcc
	v_cmp_lt_i32_e32 vcc, s31, v5
	v_lshl_or_b32 v84, v88, 7, v66
	v_lshl_or_b32 v85, v89, 7, v66
	v_cndmask_b32_e32 v90, v9, v79, vcc
	v_lshl_or_b32 v86, v90, 7, v66
	v_lshlrev_b32_e32 v88, 2, v88
	v_lshlrev_b32_e32 v89, 2, v89
	v_lshlrev_b32_e32 v90, 2, v90
	s_waitcnt vmcnt(8)
	v_cvt_pk_f16_f32 v10, v58, v59
	v_perm_b32 v11, v34, v32, s23
	v_dot2c_f32_f16_e32 v60, v11, v10
	v_perm_b32 v11, v34, v32, s24
	v_dot2c_f32_f16_e32 v42, v11, v10
	v_perm_b32 v11, v34, v32, s25
	v_dot2c_f32_f16_e32 v43, v11, v10
	v_perm_b32 v11, v34, v32, s26
	v_dot2c_f32_f16_e32 v36, v11, v10
	v_perm_b32 v11, v35, v33, s23
	v_dot2c_f32_f16_e32 v37, v11, v10
	v_perm_b32 v11, v35, v33, s24
	v_dot2c_f32_f16_e32 v30, v11, v10
	v_perm_b32 v11, v35, v33, s25
	v_dot2c_f32_f16_e32 v31, v11, v10
	v_perm_b32 v11, v35, v33, s26
	s_add_i32 s5, s5, 1
	v_dot2c_f32_f16_e32 v53, v11, v10
	s_cmp_lg_u32 s5, s4
	v_dot2c_f32_f16_e32 v45, 0x3c003c00, v10
	s_cbranch_scc1 .LBB2_43
	v_cmp_gt_i32_e32 vcc, 15, v18
	s_and_saveexec_b64 s[4:5], vcc
	s_cbranch_execz .LBB2_38
	v_max_i32_e32 v10, 1, v44
	v_cvt_f32_u32_e32 v10, v10
	v_rcp_iflag_f32_e32 v44, v10
	s_nop 0
	v_pk_mul_f32 v[10:11], v[44:45], s[2:3]
	s_nop 0
	v_mul_f32_e32 v14, 0x4b800000, v10
	v_pk_mul_f32 v[16:17], v[10:11], v[10:11] op_sel:[0,1] op_sel_hi:[1,0]
	s_nop 0
	v_fma_mixlo_f16 v15, v60, v14, v16
	v_pk_fma_f32 v[10:11], v[42:43], v[14:15], v[16:17] op_sel_hi:[1,0,0]
	v_pk_fma_f32 v[12:13], v[36:37], v[14:15], v[16:17] op_sel_hi:[1,0,0]
	v_pk_fma_f32 v[30:31], v[30:31], v[14:15], v[16:17] op_sel_hi:[1,0,0]
	v_cvt_pk_f16_f32 v11, v10, v11
	v_cvt_pk_f16_f32 v12, v12, v13
	v_cvt_pk_f16_f32 v13, v30, v31
	v_pack_b32_f16 v10, v15, v11
	v_alignbit_b32 v11, v12, v11, 16
	v_alignbit_b32 v12, v13, v12, 16
	v_lshrrev_b32_e32 v13, 16, v13
	v_fma_mixhi_f16 v13, v53, v14, v16
	v_add_u32_e32 v14, v18, v77
	v_xor_b32_e32 v15, v14, v0
	v_lshlrev_b32_e32 v15, 4, v15
	v_and_b32_e32 v15, 0xf0, v15
	v_lshl_or_b32 v14, v14, 8, v15
	ds_write_b128 v14, v[10:13]

.LBB2_49:
	s_lshl_b32 s28, s27, 2
	v_add_u32_e32 v79, s28, v3
	v_lshl_add_u32 v79, v79, 2, v2
	ds_read_b32 v80, v79 offset:15360
	ds_read_b32 v81, v79 offset:15364
	ds_read_b32 v82, v79 offset:15368
	ds_read_b32 v79, v79 offset:15372
	s_waitcnt vmcnt(10)
	v_cvt_pk_f16_f32 v10, v56, v57
	v_perm_b32 v11, v28, v26, s23
	v_dot2c_f32_f16_e32 v60, v11, v10
	v_perm_b32 v11, v28, v26, s24
	v_dot2c_f32_f16_e32 v42, v11, v10
	v_perm_b32 v11, v28, v26, s25
	v_dot2c_f32_f16_e32 v43, v11, v10
	v_perm_b32 v11, v28, v26, s26
	v_dot2c_f32_f16_e32 v36, v11, v10
	v_perm_b32 v11, v29, v27, s23
	v_dot2c_f32_f16_e32 v37, v11, v10
	v_perm_b32 v11, v29, v27, s24
	v_dot2c_f32_f16_e32 v30, v11, v10
	v_perm_b32 v11, v29, v27, s25
	v_dot2c_f32_f16_e32 v31, v11, v10
	v_perm_b32 v11, v29, v27, s26
	v_dot2c_f32_f16_e32 v53, v11, v10
	v_dot2c_f32_f16_e32 v45, 0x3c003c00, v10
	v_cmp_lt_i32_e32 vcc, s28, v5
	s_or_b32 s29, s28, 1
	s_or_b32 s30, s28, 2
	s_waitcnt lgkmcnt(0)
	v_cndmask_b32_e32 v87, v9, v80, vcc
	v_cmp_lt_i32_e32 vcc, s29, v5
	s_or_b32 s31, s28, 3
	s_nop 0
	v_cndmask_b32_e32 v88, v9, v81, vcc
	v_cmp_lt_i32_e32 vcc, s30, v5
	v_lshl_or_b32 v83, v87, 7, v66
	v_lshlrev_b32_e32 v87, 2, v87
	v_cndmask_b32_e32 v89, v9, v82, vcc
	v_cmp_lt_i32_e32 vcc, s31, v5
	v_lshl_or_b32 v84, v88, 7, v66
	v_lshl_or_b32 v85, v89, 7, v66
	v_cndmask_b32_e32 v90, v9, v79, vcc
	v_lshl_or_b32 v86, v90, 7, v66
	v_lshlrev_b32_e32 v88, 2, v88
	v_lshlrev_b32_e32 v89, 2, v89
	v_lshlrev_b32_e32 v90, 2, v90
	s_waitcnt vmcnt(8)
	v_cvt_pk_f16_f32 v10, v54, v55
	v_perm_b32 v11, v24, v22, s23
	v_dot2c_f32_f16_e32 v60, v11, v10
	v_perm_b32 v11, v24, v22, s24
	v_dot2c_f32_f16_e32 v42, v11, v10
	v_perm_b32 v11, v24, v22, s25
	v_dot2c_f32_f16_e32 v43, v11, v10
	v_perm_b32 v11, v24, v22, s26
	v_dot2c_f32_f16_e32 v36, v11, v10
	v_perm_b32 v11, v25, v23, s23
	v_dot2c_f32_f16_e32 v37, v11, v10
	v_perm_b32 v11, v25, v23, s24
	v_dot2c_f32_f16_e32 v30, v11, v10
	v_perm_b32 v11, v25, v23, s25
	v_dot2c_f32_f16_e32 v31, v11, v10
	v_perm_b32 v11, v25, v23, s26
	s_add_i32 s5, s5, 1
	v_dot2c_f32_f16_e32 v53, v11, v10
	s_cmp_lg_u32 s5, s4
	v_dot2c_f32_f16_e32 v45, 0x3c003c00, v10
	s_cbranch_scc1 .LBB2_57
	v_cmp_gt_i32_e32 vcc, 15, v18
	s_and_saveexec_b64 s[4:5], vcc
	s_cbranch_execz .LBB2_52
	v_max_i32_e32 v10, 1, v44
	v_cvt_f32_u32_e32 v10, v10
	v_rcp_iflag_f32_e32 v44, v10
	s_nop 0
	v_pk_mul_f32 v[10:11], v[44:45], s[2:3]
	s_nop 0
	v_mul_f32_e32 v14, 0x4b800000, v10
	v_pk_mul_f32 v[16:17], v[10:11], v[10:11] op_sel:[0,1] op_sel_hi:[1,0]
	s_nop 0
	v_fma_mixlo_f16 v15, v60, v14, v16
	v_pk_fma_f32 v[10:11], v[42:43], v[14:15], v[16:17] op_sel_hi:[1,0,0]
	v_pk_fma_f32 v[12:13], v[36:37], v[14:15], v[16:17] op_sel_hi:[1,0,0]
	v_pk_fma_f32 v[22:23], v[30:31], v[14:15], v[16:17] op_sel_hi:[1,0,0]
	v_cvt_pk_f16_f32 v11, v10, v11
	v_cvt_pk_f16_f32 v12, v12, v13
	v_cvt_pk_f16_f32 v13, v22, v23
	v_pack_b32_f16 v10, v15, v11
	v_alignbit_b32 v11, v12, v11, 16
	v_alignbit_b32 v12, v13, v12, 16
	v_lshrrev_b32_e32 v13, 16, v13
	v_fma_mixhi_f16 v13, v53, v14, v16
	v_add_u32_e32 v14, v18, v77
	v_xor_b32_e32 v15, v14, v0
	v_lshlrev_b32_e32 v15, 4, v15
	v_and_b32_e32 v15, 0xf0, v15
	v_lshl_or_b32 v14, v14, 8, v15
	ds_write_b128 v14, v[10:13]

.LBB3_33:
	s_lshl_b32 s26, s25, 2
	v_add_u32_e32 v82, s26, v3
	v_lshl_add_u32 v82, v82, 2, v2
	ds_read_b32 v83, v82 offset:15360
	ds_read_b32 v84, v82 offset:15364
	ds_read_b32 v85, v82 offset:15368
	ds_read_b32 v82, v82 offset:15372
	s_waitcnt vmcnt(10)
	v_cvt_pk_f16_f32 v9, v57, v58
	v_perm_b32 v10, v40, v38, s21
	v_dot2c_f32_f16_e32 v56, v10, v9
	v_perm_b32 v10, v40, v38, s22
	v_dot2c_f32_f16_e32 v42, v10, v9
	v_perm_b32 v10, v40, v38, s23
	v_dot2c_f32_f16_e32 v43, v10, v9
	v_perm_b32 v10, v40, v38, s24
	v_dot2c_f32_f16_e32 v36, v10, v9
	v_perm_b32 v10, v41, v39, s21
	v_dot2c_f32_f16_e32 v37, v10, v9
	v_perm_b32 v10, v41, v39, s22
	v_dot2c_f32_f16_e32 v30, v10, v9
	v_perm_b32 v10, v41, v39, s23
	v_dot2c_f32_f16_e32 v31, v10, v9
	v_perm_b32 v10, v41, v39, s24
	v_dot2c_f32_f16_e32 v49, v10, v9
	v_cmp_lt_i32_e32 vcc, s26, v5
	s_or_b32 s28, s26, 1
	s_or_b32 s29, s26, 2
	s_waitcnt lgkmcnt(0)
	v_cndmask_b32_e32 v87, v8, v83, vcc
	v_cmp_lt_i32_e32 vcc, s28, v5
	s_or_b32 s30, s26, 3
	s_nop 0
	v_cndmask_b32_e32 v88, v8, v84, vcc
	v_cmp_lt_i32_e32 vcc, s29, v5
	v_lshl_or_b32 v79, v87, 7, v78
	v_lshlrev_b32_e32 v87, 2, v87
	v_cndmask_b32_e32 v89, v8, v85, vcc
	v_cmp_lt_i32_e32 vcc, s30, v5
	v_lshl_or_b32 v80, v88, 7, v78
	v_lshl_or_b32 v81, v89, 7, v78
	v_cndmask_b32_e32 v90, v8, v82, vcc
	v_lshl_or_b32 v86, v90, 7, v78
	v_lshlrev_b32_e32 v88, 2, v88
	v_lshlrev_b32_e32 v89, 2, v89
	v_lshlrev_b32_e32 v90, 2, v90
	s_waitcnt vmcnt(8)
	v_cvt_pk_f16_f32 v9, v54, v55
	v_perm_b32 v10, v34, v32, s21
	v_dot2c_f32_f16_e32 v56, v10, v9
	v_perm_b32 v10, v34, v32, s22
	v_dot2c_f32_f16_e32 v42, v10, v9
	v_perm_b32 v10, v34, v32, s23
	v_dot2c_f32_f16_e32 v43, v10, v9
	v_perm_b32 v10, v34, v32, s24
	v_dot2c_f32_f16_e32 v36, v10, v9
	v_perm_b32 v10, v35, v33, s21
	v_dot2c_f32_f16_e32 v37, v10, v9
	v_perm_b32 v10, v35, v33, s22
	v_dot2c_f32_f16_e32 v30, v10, v9
	v_perm_b32 v10, v35, v33, s23
	v_dot2c_f32_f16_e32 v31, v10, v9
	v_perm_b32 v10, v35, v33, s24
	s_add_i32 s5, s5, 1
	v_dot2c_f32_f16_e32 v49, v10, v9
	s_cmp_lg_u32 s5, s4
	s_cbranch_scc1 .LBB3_41
	v_cmp_gt_i32_e32 vcc, 15, v18
	s_and_saveexec_b64 s[4:5], vcc
	s_cbranch_execz .LBB3_36
	v_max_i32_e32 v9, 1, v44
	v_cvt_f32_u32_e32 v9, v9
	v_rcp_iflag_f32_e32 v44, v9
	s_nop 0
	v_pk_mul_f32 v[10:11], v[44:45], s[2:3]
	s_nop 0
	v_mul_f32_e32 v14, 0x4b800000, v10
	v_pk_mul_f32 v[16:17], v[10:11], v[10:11] op_sel:[0,1] op_sel_hi:[1,0]
	s_nop 0
	v_pk_fma_f32 v[10:11], v[42:43], v[14:15], v[16:17] op_sel_hi:[1,0,0]
	v_fma_mixlo_f16 v9, v56, v14, v16
	v_pk_fma_f32 v[12:13], v[36:37], v[14:15], v[16:17] op_sel_hi:[1,0,0]
	v_pk_fma_f32 v[30:31], v[30:31], v[14:15], v[16:17] op_sel_hi:[1,0,0]
	v_cvt_pk_f16_f32 v11, v10, v11
	v_cvt_pk_f16_f32 v12, v12, v13
	v_pack_b32_f16 v10, v9, v11
	v_cvt_pk_f16_f32 v9, v30, v31
	v_alignbit_b32 v11, v12, v11, 16
	v_alignbit_b32 v12, v9, v12, 16
	v_lshrrev_b32_e32 v13, 16, v9
	v_add_u32_e32 v9, v18, v75
	v_fma_mixhi_f16 v13, v49, v14, v16
	v_xor_b32_e32 v14, v9, v0
	v_lshlrev_b32_e32 v14, 4, v14
	v_and_b32_e32 v14, 0xf0, v14
	v_lshl_or_b32 v9, v9, 8, v14
	ds_write_b128 v9, v[10:13]

.LBB3_47:
	s_lshl_b32 s26, s25, 2
	v_add_u32_e32 v82, s26, v3
	v_lshl_add_u32 v82, v82, 2, v2
	ds_read_b32 v83, v82 offset:15360
	ds_read_b32 v84, v82 offset:15364
	ds_read_b32 v85, v82 offset:15368
	ds_read_b32 v82, v82 offset:15372
	s_waitcnt vmcnt(10)
	v_cvt_pk_f16_f32 v9, v52, v53
	v_perm_b32 v10, v28, v26, s21
	v_dot2c_f32_f16_e32 v56, v10, v9
	v_perm_b32 v10, v28, v26, s22
	v_dot2c_f32_f16_e32 v42, v10, v9
	v_perm_b32 v10, v28, v26, s23
	v_dot2c_f32_f16_e32 v43, v10, v9
	v_perm_b32 v10, v28, v26, s24
	v_dot2c_f32_f16_e32 v36, v10, v9
	v_perm_b32 v10, v29, v27, s21
	v_dot2c_f32_f16_e32 v37, v10, v9
	v_perm_b32 v10, v29, v27, s22
	v_dot2c_f32_f16_e32 v30, v10, v9
	v_perm_b32 v10, v29, v27, s23
	v_dot2c_f32_f16_e32 v31, v10, v9
	v_perm_b32 v10, v29, v27, s24
	v_dot2c_f32_f16_e32 v49, v10, v9
	v_cmp_lt_i32_e32 vcc, s26, v5
	s_or_b32 s28, s26, 1
	s_or_b32 s29, s26, 2
	s_waitcnt lgkmcnt(0)
	v_cndmask_b32_e32 v87, v8, v83, vcc
	v_cmp_lt_i32_e32 vcc, s28, v5
	s_or_b32 s30, s26, 3
	s_nop 0
	v_cndmask_b32_e32 v88, v8, v84, vcc
	v_cmp_lt_i32_e32 vcc, s29, v5
	v_lshl_or_b32 v79, v87, 7, v78
	v_lshlrev_b32_e32 v87, 2, v87
	v_cndmask_b32_e32 v89, v8, v85, vcc
	v_cmp_lt_i32_e32 vcc, s30, v5
	v_lshl_or_b32 v80, v88, 7, v78
	v_lshl_or_b32 v81, v89, 7, v78
	v_cndmask_b32_e32 v90, v8, v82, vcc
	v_lshl_or_b32 v86, v90, 7, v78
	v_lshlrev_b32_e32 v88, 2, v88
	v_lshlrev_b32_e32 v89, 2, v89
	v_lshlrev_b32_e32 v90, 2, v90
	s_waitcnt vmcnt(8)
	v_cvt_pk_f16_f32 v9, v50, v51
	v_perm_b32 v10, v24, v22, s21
	v_dot2c_f32_f16_e32 v56, v10, v9
	v_perm_b32 v10, v24, v22, s22
	v_dot2c_f32_f16_e32 v42, v10, v9
	v_perm_b32 v10, v24, v22, s23
	v_dot2c_f32_f16_e32 v43, v10, v9
	v_perm_b32 v10, v24, v22, s24
	v_dot2c_f32_f16_e32 v36, v10, v9
	v_perm_b32 v10, v25, v23, s21
	v_dot2c_f32_f16_e32 v37, v10, v9
	v_perm_b32 v10, v25, v23, s22
	v_dot2c_f32_f16_e32 v30, v10, v9
	v_perm_b32 v10, v25, v23, s23
	v_dot2c_f32_f16_e32 v31, v10, v9
	v_perm_b32 v10, v25, v23, s24
	s_add_i32 s5, s5, 1
	v_dot2c_f32_f16_e32 v49, v10, v9
	s_cmp_lg_u32 s5, s4
	s_cbranch_scc1 .LBB3_55
	v_cmp_gt_i32_e32 vcc, 15, v18
	s_and_saveexec_b64 s[4:5], vcc
	s_cbranch_execz .LBB3_50
	v_max_i32_e32 v9, 1, v44
	v_cvt_f32_u32_e32 v9, v9
	v_rcp_iflag_f32_e32 v44, v9
	s_nop 0
	v_pk_mul_f32 v[10:11], v[44:45], s[2:3]
	s_nop 0
	v_mul_f32_e32 v14, 0x4b800000, v10
	v_pk_mul_f32 v[16:17], v[10:11], v[10:11] op_sel:[0,1] op_sel_hi:[1,0]
	s_nop 0
	v_pk_fma_f32 v[10:11], v[42:43], v[14:15], v[16:17] op_sel_hi:[1,0,0]
	v_fma_mixlo_f16 v9, v56, v14, v16
	v_pk_fma_f32 v[12:13], v[36:37], v[14:15], v[16:17] op_sel_hi:[1,0,0]
	v_pk_fma_f32 v[22:23], v[30:31], v[14:15], v[16:17] op_sel_hi:[1,0,0]
	v_cvt_pk_f16_f32 v11, v10, v11
	v_cvt_pk_f16_f32 v12, v12, v13
	v_pack_b32_f16 v10, v9, v11
	v_cvt_pk_f16_f32 v9, v22, v23
	v_alignbit_b32 v11, v12, v11, 16
	v_alignbit_b32 v12, v9, v12, 16
	v_lshrrev_b32_e32 v13, 16, v9
	v_add_u32_e32 v9, v18, v75
	v_fma_mixhi_f16 v13, v49, v14, v16
	v_xor_b32_e32 v14, v9, v0
	v_lshlrev_b32_e32 v14, 4, v14
	v_and_b32_e32 v14, 0xf0, v14
	v_lshl_or_b32 v9, v9, 8, v14
	ds_write_b128 v9, v[10:13]
